# baseline (speedup 1.0000x reference)
.LBB2_12:
	s_or_b64 exec, exec, s[12:13]
	v_lshlrev_b32_e32 v106, 9, v119
	v_ffbl_b32_e32 v107, v107
	v_ffbl_b32_e32 v108, v108
	v_lshlrev_b32_e32 v116, 25, v119
	v_lshl_or_b32 v107, v107, 4, v106
	v_mov_b32_e32 v109, 0x2000
	v_lshl_or_b32 v108, v108, 20, v116
	v_bfrev_b32_e32 v116, 4
	v_ffbl_b32_e32 v0, v0
	v_cndmask_b32_e64 v107, v107, v109, s[8:9]
	v_cndmask_b32_e64 v108, v108, v116, s[4:5]
	v_lshl_or_b32 v0, v0, 4, v106
	v_cndmask_b32_e32 v0, v0, v109, vcc
	v_or_b32_e32 v106, v108, v107
	v_mov_b32_e32 v108, 0x800000
	v_lshlrev_b32_e32 v107, 16, v117
	v_cndmask_b32_e64 v108, 0, v108, s[6:7]
	s_waitcnt lgkmcnt(2)
	v_lshl_or_b32 v0, v118, 24, v0
	v_or3_b32 v0, v0, v108, v107
	ds_write2_b32 v105, v106, v0 offset0:1 offset1:3
	v_cmp_ne_u32_e32 vcc, 0, v140
	v_cmp_ne_u32_e64 s[22:23], 0, v141
	v_lshlrev_b32_e32 v150, 5, v113
	v_lshl_add_u32 v155, v113, 2, v115
	v_lshlrev_b32_e32 v155, 2, v155
	v_add_u32_e32 v155, 0x11840, v155
	v_lshrrev_b64 v[146:147], v150, vcc
	v_lshrrev_b64 v[156:157], v150, s[22:23]
	v_mov_b32_e32 v151, 0x400
	v_cmp_ne_u32_e32 vcc, 0, v146
	v_cmp_ne_u32_e64 s[22:23], 0, v156
	s_nop 1
	v_cndmask_b32_e32 v146, 0, v151, vcc
	v_cndmask_b32_e64 v156, 0, v151, s[22:23]
	v_cmp_eq_u32_e32 vcc, 0, v111
	s_and_saveexec_b64 s[22:23], vcc
	ds_or_b32 v155, v146
	ds_or_b32 v155, v156 offset:32
	s_or_b64 exec, exec, s[22:23]
	s_movk_i32 s2, 0x2010
	v_mul_u32_u24_e32 v105, 0x2010, v115
	v_cmp_eq_u32_e32 vcc, 0, v114
	s_waitcnt vmcnt(22)
	ds_write_b128 v104, v[38:41] offset:32832
	s_waitcnt vmcnt(21)
	ds_write_b128 v104, v[42:45] offset:36928
	s_waitcnt vmcnt(20)
	ds_write_b128 v104, v[46:49] offset:41024
	s_waitcnt vmcnt(19)
	ds_write_b128 v104, v[50:53] offset:45120
	s_waitcnt vmcnt(18)
	ds_write_b128 v104, v[54:57] offset:49216
	s_waitcnt vmcnt(17)
	ds_write_b128 v104, v[66:69] offset:53312
	s_and_saveexec_b64 s[0:1], vcc
	v_mov_b32_e32 v38, 0
	v_mov_b32_e32 v39, v38
	v_mov_b32_e32 v40, v38
	v_mov_b32_e32 v41, v38
	ds_write_b128 v105, v[38:41] offset:8192
	s_or_b64 exec, exec, s[0:1]
	v_lshlrev_b32_e32 v40, 3, v113
	v_lshlrev_b32_e32 v67, 4, v110
	v_or_b32_e32 v38, 0x1e0, v111
	v_or_b32_e32 v0, 0x8040, v40
	v_mad_u32_u24 v66, v1, s2, v67
	v_mad_u32_u24 v38, v38, 48, v0
	s_waitcnt vmcnt(16)
	ds_write_b128 v66, v[58:61]
	s_waitcnt vmcnt(15)
	ds_write_b128 v66, v[62:65] offset:1024
	s_waitcnt vmcnt(14)
	ds_write_b128 v66, v[70:73] offset:2048
	s_waitcnt vmcnt(13)
	ds_write_b128 v66, v[74:77] offset:3072
	s_waitcnt vmcnt(12)
	ds_write_b128 v66, v[78:81] offset:4096
	s_waitcnt vmcnt(11)
	ds_write_b128 v66, v[82:85] offset:5120
	s_waitcnt vmcnt(10)
	ds_write_b128 v66, v[86:89] offset:6144
	s_waitcnt vmcnt(9)
	ds_write_b128 v66, v[90:93] offset:7168
	v_lshl_add_u32 v116, v113, 3, v105
	v_or_b32_e32 v106, 0x1e0, v111
	v_lshlrev_b32_e32 v138, 4, v106
	v_lshlrev_b32_e32 v139, 3, v106
	v_add_u32_e32 v139, 0x118c0, v139
	v_mul_u32_u24_e32 v156, 48, v106
	v_add_u32_e32 v156, v0, v156
	v_mov_b32_e32 v157, 0x1187c
	v_add_u32_e32 v137, v116, v138
	v_add_u32_e32 v138, 0x200, v138
	v_lshlrev_b32_e32 v160, 4, v111
	v_lshlrev_b32_e32 v161, 3, v111
	v_add_u32_e32 v161, 0x118c0, v161
	v_mul_u32_u24_e32 v162, 48, v111
	v_add_u32_e32 v162, v0, v162
	v_mov_b32_e32 v163, 0x11840
	v_mul_hi_u32_u24_e32 v159, 0x410, v111
	v_mul_u32_u24_e32 v158, 0x410, v111
	v_mov_b32_e32 v107, 0x82000
	v_mad_u64_u32 v[158:159], s[0:1], s20, v107, v[158:159]
	v_lshlrev_b32_e32 v107, 3, v113
	v_or_b32_e32 v158, v158, v107
	v_lshl_add_u64 v[158:159], s[14:15], 0, v[158:159]
	s_mov_b64 s[0:1], 0x79e30
	s_mov_b32 s2, 0xffff7e00
	s_mov_b32 s3, -1
	v_lshl_add_u64 v[158:159], v[158:159], 0, s[0:1]
	v_lshl_add_u32 v107, v114, 2, v163
	v_add_u32_e32 v107, -8, v107
	s_waitcnt lgkmcnt(0)
	s_barrier
	ds_read_b128 v[38:41], v138 offset:56896
	ds_read_b64 v[42:43], v139
	ds_read2_b64 v[56:59], v156 offset1:2
	ds_read_b32 v60, v107
	v_add_u32_e32 v156, 0xfffffa00, v156
	ds_read2_b64 v[52:55], v156 offset1:2
	v_add_u32_e32 v106, -2, v114
	v_cmp_gt_u32_e32 vcc, 16, v106
	s_waitcnt lgkmcnt(0)
	v_cndmask_b32_e32 v60, 0, v60, vcc
	s_nop 1
	v_readlane_b32 s4, v60, 17
	v_readlane_b32 s21, v60, 16
	v_add_u32_sdwa v92, v105, v56 dst_sel:DWORD dst_unused:UNUSED_PAD src0_sel:DWORD src1_sel:WORD_0
	v_add_u32_sdwa v93, v105, v56 dst_sel:DWORD dst_unused:UNUSED_PAD src0_sel:DWORD src1_sel:WORD_1
	v_add_u32_sdwa v106, v105, v57 dst_sel:DWORD dst_unused:UNUSED_PAD src0_sel:DWORD src1_sel:WORD_0
	v_add_u32_sdwa v107, v105, v57 dst_sel:DWORD dst_unused:UNUSED_PAD src0_sel:DWORD src1_sel:WORD_1
	v_add_u32_sdwa v108, v105, v58 dst_sel:DWORD dst_unused:UNUSED_PAD src0_sel:DWORD src1_sel:WORD_0
	v_add_u32_sdwa v109, v105, v58 dst_sel:DWORD dst_unused:UNUSED_PAD src0_sel:DWORD src1_sel:WORD_1
	v_add_u32_sdwa v88, v105, v59 dst_sel:DWORD dst_unused:UNUSED_PAD src0_sel:DWORD src1_sel:WORD_0
	v_add_u32_sdwa v89, v105, v59 dst_sel:DWORD dst_unused:UNUSED_PAD src0_sel:DWORD src1_sel:WORD_1
	ds_read_b128 v[120:123], v92
	ds_read_b128 v[124:127], v93
	ds_read_b128 v[128:131], v106
	ds_read_b128 v[132:135], v107
	ds_read_b128 v[140:143], v108
	ds_read_b128 v[144:147], v109
	ds_read_b128 v[148:151], v88
	ds_read_b128 v[152:155], v89
	v_add_u32_sdwa v88, v116, v42 dst_sel:DWORD dst_unused:UNUSED_PAD src0_sel:DWORD src1_sel:WORD_0
	v_add_u32_sdwa v89, v116, v42 dst_sel:DWORD dst_unused:UNUSED_PAD src0_sel:DWORD src1_sel:WORD_1
	v_add_u32_sdwa v90, v116, v43 dst_sel:DWORD dst_unused:UNUSED_PAD src0_sel:DWORD src1_sel:WORD_0
	v_add_u32_sdwa v91, v116, v43 dst_sel:DWORD dst_unused:UNUSED_PAD src0_sel:DWORD src1_sel:WORD_1
	v_bfe_u32 v117, v41, 16, 7
	v_add_u32_sdwa v118, v116, v39 dst_sel:DWORD dst_unused:UNUSED_PAD src0_sel:DWORD src1_sel:WORD_0
	v_add_u32_sdwa v119, v116, v39 dst_sel:DWORD dst_unused:UNUSED_PAD src0_sel:DWORD src1_sel:WORD_1
	v_add_u32_sdwa v136, v116, v41 dst_sel:DWORD dst_unused:UNUSED_PAD src0_sel:DWORD src1_sel:WORD_0
	s_or_b32 s10, s4, s21
	s_and_b32 s10, s10, 0x700
	s_and_b32 s9, s4, 0xff
	s_cselect_b32 s24, 0, 0x700
	s_or_b32 s10, s10, s24
	s_waitcnt lgkmcnt(0)
	v_pk_add_f32 v[120:121], v[120:121], v[124:125]
	v_pk_add_f32 v[122:123], v[122:123], v[126:127]
	v_pk_add_f32 v[128:129], v[128:129], v[132:133]
	v_pk_add_f32 v[130:131], v[130:131], v[134:135]
	v_pk_add_f32 v[140:141], v[140:141], v[144:145]
	v_pk_add_f32 v[142:143], v[142:143], v[146:147]
	v_pk_add_f32 v[148:149], v[148:149], v[152:153]
	v_pk_add_f32 v[150:151], v[150:151], v[154:155]
	s_bitcmp1_b32 s4, 8
	s_cbranch_scc1 .Lfarslow_pre
.Lfarslow_ret_pre:
	v_pk_add_f32 v[120:121], v[120:121], v[128:129]
	v_pk_add_f32 v[122:123], v[122:123], v[130:131]
	v_pk_add_f32 v[140:141], v[140:141], v[148:149]
	v_pk_add_f32 v[142:143], v[142:143], v[150:151]
	v_pk_add_f32 v[120:121], v[120:121], v[140:141]
	v_pk_add_f32 v[122:123], v[122:123], v[142:143]
	s_nop 1
	v_permlane32_swap_b32_e32 v120, v122
	v_permlane32_swap_b32_e32 v121, v123
	v_pk_add_f32 v[44:45], v[120:121], v[122:123]
	v_add_u32_e32 v138, 0xfffffe00, v138
	v_add_u32_e32 v139, 0xffffff00, v139
	v_add_u32_e32 v156, 0xfffffa00, v156
	v_lshl_add_u64 v[158:159], v[158:159], 0, s[2:3]
	s_mov_b32 s5, 15
	s_mov_b32 s5, 15
	s_cmp_lg_u32 s10, 0
	s_cbranch_scc1 .Lit_As

.Lfarslow_pre:
	s_waitcnt lgkmcnt(0)
	ds_read_b64 v[64:65], v156 offset:1568
	v_and_b32_e32 v164, 0x3ff, v38
	v_mov_b64_e32 v[166:167], v[158:159]
	s_movk_i32 s22, 24
	s_waitcnt lgkmcnt(0)
.Lfs_gather_pre:
	v_add_u32_sdwa v92, v105, v64 dst_sel:DWORD dst_unused:UNUSED_PAD src0_sel:DWORD src1_sel:WORD_0
	v_add_u32_sdwa v93, v105, v64 dst_sel:DWORD dst_unused:UNUSED_PAD src0_sel:DWORD src1_sel:WORD_1
	v_add_u32_sdwa v106, v105, v65 dst_sel:DWORD dst_unused:UNUSED_PAD src0_sel:DWORD src1_sel:WORD_0
	v_add_u32_sdwa v107, v105, v65 dst_sel:DWORD dst_unused:UNUSED_PAD src0_sel:DWORD src1_sel:WORD_1
	ds_read_b128 v[124:127], v92
	ds_read_b128 v[132:135], v93
	ds_read_b128 v[144:147], v106
	ds_read_b128 v[152:155], v107
	s_waitcnt lgkmcnt(0)
	v_pk_add_f32 v[124:125], v[124:125], v[132:133]
	v_pk_add_f32 v[126:127], v[126:127], v[134:135]
	v_pk_add_f32 v[144:145], v[144:145], v[152:153]
	v_pk_add_f32 v[146:147], v[146:147], v[154:155]
	v_pk_add_f32 v[124:125], v[124:125], v[144:145]
	v_pk_add_f32 v[126:127], v[126:127], v[146:147]
	s_nop 0
	v_pk_add_f32 v[148:149], v[148:149], v[124:125]
	v_pk_add_f32 v[150:151], v[150:151], v[126:127]
	v_cmp_lt_u32_e32 vcc, s22, v164
	s_cbranch_vccz .Lfarslow_ret_pre
	v_add_u32_e32 v165, s22, v112
	v_cmp_lt_u32_e32 vcc, v165, v164
	v_mov_b32_e32 v64, 0x20002000
	v_mov_b32_e32 v65, 0x20002000
	s_and_saveexec_b64 s[12:13], vcc
	global_load_dwordx2 v[64:65], v[166:167], off
	s_mov_b64 exec, -1
	v_lshl_add_u64 v[166:167], v[166:167], 0, 16
	s_add_i32 s22, s22, 8
	s_waitcnt vmcnt(0)
	s_branch .Lfs_gather_pre
.Lfarslow_As:
	s_waitcnt lgkmcnt(0)
	ds_read_b64 v[64:65], v156 offset:1568
	v_and_b32_e32 v164, 0x3ff, v46
	v_mov_b64_e32 v[166:167], v[158:159]
	s_movk_i32 s22, 24
	s_waitcnt lgkmcnt(0)
